# nca kernels: partner-partial LDS reads hoisted directly behind the exchange barrier (merge scalars moved to spare VGPRs), waits recounted
# baseline (speedup 1.0000x reference)
.LBB1_22:
	s_or_b64 exec, exec, s[0:1]
	s_add_i32 s0, 0, 0x11880
	s_movk_i32 s1, 0x1600
	v_mov_b32_e32 v7, s0
	v_mad_u32_u24 v8, v6, s1, v7
	v_lshlrev_b32_e32 v9, 2, v39
	v_xor_b32_e32 v6, 4, v6
	v_add_u32_e32 v27, v8, v9
	v_mad_u32_u24 v6, v6, s1, v7
	ds_write2st64_b32 v27, v22, v23 offset1:1
	ds_write2st64_b32 v27, v24, v25 offset0:2 offset1:3
	ds_write2st64_b32 v27, v18, v19 offset0:4 offset1:5
	ds_write2st64_b32 v27, v20, v21 offset0:6 offset1:7
	ds_write2st64_b32 v27, v14, v15 offset0:8 offset1:9
	ds_write2st64_b32 v27, v16, v17 offset0:10 offset1:11
	ds_write2st64_b32 v27, v10, v11 offset0:12 offset1:13
	ds_write2st64_b32 v27, v12, v13 offset0:14 offset1:15
	ds_write2st64_b32 v27, v2, v3 offset0:16 offset1:17
	ds_write2st64_b32 v27, v4, v5 offset0:18 offset1:19
	ds_write_b32 v27, v26 offset:5120
	v_add_u32_e32 v27, v6, v9
	s_waitcnt lgkmcnt(0)
	s_barrier
	ds_read_b32 v122, v27 offset:5120
	v_lshlrev_b32_e32 v7, 2, v40
	v_add_u32_e32 v8, v8, v7
	v_add_u32_e32 v6, v6, v7
	ds_read_b32 v121, v6 offset:4224
	ds_read_b32 v120, v8 offset:4224
	ds_read2st64_b32 v[32:33], v27 offset0:18 offset1:19
	ds_read2st64_b32 v[34:35], v27 offset0:16 offset1:17
	ds_read2st64_b32 v[6:7], v27 offset1:1
	ds_read2st64_b32 v[8:9], v27 offset0:2 offset1:3
	ds_read2st64_b32 v[42:43], v27 offset0:4 offset1:5
	ds_read2st64_b32 v[44:45], v27 offset0:6 offset1:7
	ds_read2st64_b32 v[46:47], v27 offset0:8 offset1:9
	ds_read2st64_b32 v[48:49], v27 offset0:10 offset1:11
	ds_read2st64_b32 v[50:51], v27 offset0:12 offset1:13
	ds_read2st64_b32 v[52:53], v27 offset0:14 offset1:15
	s_waitcnt lgkmcnt(12)
	v_max_f32_e32 v123, v122, v122
	v_max_f32_e32 v28, v26, v26
	v_max_f32_e32 v28, v28, v123
	v_sub_f32_e32 v124, v26, v28
	v_sub_f32_e32 v125, v122, v28
	v_exp_f32_e32 v124, v124
	v_exp_f32_e32 v125, v125
	s_movk_i32 s0, 0x100
	s_add_i32 s1, 0, 0x10e00
	v_lshl_add_u32 v26, v38, 2, s1
	s_waitcnt lgkmcnt(10)
	v_pk_mul_f32 v[120:121], v[120:121], v[124:125]
	v_cmp_gt_u32_e64 s[0:1], s0, v0
	v_add_f32_e32 v126, v120, v121
	v_rcp_f32_e32 v126, v126
	v_cndmask_b32_e64 v56, 48, 0, s[0:1]
	v_lshl_add_u32 v41, v56, 2, v26
	ds_read_b128 v[28:31], v41
	v_mul_f32_e32 v36, v124, v126
	v_mul_f32_e32 v40, v125, v126
	s_waitcnt lgkmcnt(8)
	v_pk_mul_f32 v[6:7], v[40:41], v[6:7] op_sel_hi:[0,1]
	s_waitcnt lgkmcnt(7)
	v_pk_mul_f32 v[8:9], v[40:41], v[8:9] op_sel_hi:[0,1]
	v_pk_fma_f32 v[6:7], v[36:37], v[22:23], v[6:7] op_sel_hi:[0,1,1]
	v_pk_fma_f32 v[8:9], v[36:37], v[24:25], v[8:9] op_sel_hi:[0,1,1]
	v_cvt_pk_f16_f32 v6, v6, v7
	v_cvt_pk_f16_f32 v7, v8, v9
	s_waitcnt lgkmcnt(6)
	v_pk_mul_f32 v[8:9], v[40:41], v[42:43] op_sel_hi:[0,1]
	v_pk_fma_f32 v[8:9], v[36:37], v[18:19], v[8:9] op_sel_hi:[0,1,1]
	s_waitcnt lgkmcnt(5)
	v_pk_mul_f32 v[18:19], v[40:41], v[44:45] op_sel_hi:[0,1]
	v_pk_fma_f32 v[18:19], v[36:37], v[20:21], v[18:19] op_sel_hi:[0,1,1]
	v_cvt_pk_f16_f32 v8, v8, v9
	v_cvt_pk_f16_f32 v9, v18, v19
	s_waitcnt lgkmcnt(4)
	v_pk_mul_f32 v[18:19], v[40:41], v[46:47] op_sel_hi:[0,1]
	v_pk_fma_f32 v[14:15], v[36:37], v[14:15], v[18:19] op_sel_hi:[0,1,1]
	s_waitcnt lgkmcnt(3)
	v_pk_mul_f32 v[18:19], v[40:41], v[48:49] op_sel_hi:[0,1]
	v_pk_fma_f32 v[16:17], v[36:37], v[16:17], v[18:19] op_sel_hi:[0,1,1]
	v_cvt_pk_f16_f32 v14, v14, v15
	v_cvt_pk_f16_f32 v15, v16, v17
	s_waitcnt lgkmcnt(2)
	v_pk_mul_f32 v[16:17], v[40:41], v[50:51] op_sel_hi:[0,1]
	v_pk_fma_f32 v[10:11], v[36:37], v[10:11], v[16:17] op_sel_hi:[0,1,1]
	v_cvt_pk_f16_f32 v16, v10, v11
	s_waitcnt lgkmcnt(0)
	v_pk_mul_f32 v[10:11], v[40:41], v[52:53] op_sel_hi:[0,1]
	v_lshlrev_b32_e32 v0, 2, v0
	v_pk_fma_f32 v[10:11], v[36:37], v[12:13], v[10:11] op_sel_hi:[0,1,1]
	v_and_b32_e32 v20, 12, v0
	v_cvt_pk_f16_f32 v17, v10, v11
	v_pk_mul_f32 v[10:11], v[40:41], v[34:35] op_sel_hi:[0,1]
	v_or_b32_e32 v0, v56, v20
	v_pk_fma_f32 v[2:3], v[36:37], v[2:3], v[10:11] op_sel_hi:[0,1,1]
	v_lshlrev_b32_e32 v27, 1, v0
	v_or_b32_e32 v0, v1, v38
	v_cvt_pk_f16_f32 v10, v2, v3
	v_pk_mul_f32 v[2:3], v[40:41], v[32:33] op_sel_hi:[0,1]
	v_mul_u32_u24_e32 v0, 0x50, v0
	v_pk_fma_f32 v[2:3], v[36:37], v[4:5], v[2:3] op_sel_hi:[0,1,1]
	v_lshlrev_b32_e32 v21, 1, v0
	v_cvt_pk_f16_f32 v2, v2, v3
	v_cmp_gt_u32_e32 vcc, 32, v39
	v_add3_u32 v42, 0, v27, v21
	v_add_u32_e32 v22, 0, v21
	v_cndmask_b32_e32 v25, 0, v2, vcc
	v_add_u32_e32 v43, v22, v27
	ds_read_b64_tr_b16 v[2:3], v42 offset:57600
	ds_read_b64_tr_b16 v[4:5], v43 offset:60160
	v_and_or_b32 v0, v38, 4, v1
	s_movk_i32 s4, 0xa0
	v_mad_u32_u24 v0, v0, s4, 0
	v_add_u32_e32 v23, 0xe100, v0
	v_lshl_add_u64 v[18:19], v[54:55], 1, s[2:3]
	v_lshlrev_b32_e32 v32, 1, v38
	v_mov_b32_e32 v33, 0
	s_waitcnt lgkmcnt(0)
	v_mfma_f32_16x16x32_f16 v[0:3], v[2:5], v[6:9], v[28:31]
	v_lshl_add_u64 v[4:5], v[18:19], 0, v[32:33]
	v_add_u32_e32 v18, v23, v27
	v_cndmask_b32_e32 v24, 0, v10, vcc
	ds_read_b64_tr_b16 v[12:13], v43 offset:65280
	ds_read_b64_tr_b16 v[10:11], v42 offset:62720
	ds_read_b64_tr_b16 v[30:31], v18 offset:10240
	v_mov_b32_e32 v32, v33
	ds_read_b64_tr_b16 v[34:35], v42 offset:57632
	ds_read_b64_tr_b16 v[36:37], v43 offset:60192
	ds_read_b128 v[38:41], v41 offset:64
	s_waitcnt lgkmcnt(4)
	v_mfma_f32_16x16x32_f16 v[10:13], v[10:13], v[14:17], v[0:3]
	s_mov_b32 s2, 0xffff
	s_or_b64 s[4:5], s[0:1], vcc
	s_nop 0
	v_bfi_b32 v0, s2, v24, v24
	v_bfi_b32 v1, s2, v25, v25
	v_mov_b32_e32 v2, v33
	v_mov_b32_e32 v3, v33
	s_waitcnt lgkmcnt(0)
	v_mfma_f32_16x16x32_f16 v[34:37], v[34:37], v[6:9], v[38:41]
	v_mfma_f32_16x16x32_f16 v[10:13], v[30:33], v[0:3], v[10:13]
	ds_read_b64_tr_b16 v[44:45], v43 offset:65312
	ds_read_b64_tr_b16 v[42:43], v42 offset:62752
	ds_read_b64_tr_b16 v[30:31], v18 offset:10272
	v_lshlrev_b32_e32 v32, 1, v56
	v_lshl_add_u64 v[18:19], v[4:5], 0, v[32:33]
	v_mov_b32_e32 v32, v33
	s_waitcnt lgkmcnt(1)
	v_mfma_f32_16x16x32_f16 v[34:37], v[42:45], v[14:17], v[34:37]
	v_cvt_pk_f16_f32 v13, v12, v13
	v_cvt_pk_f16_f32 v12, v10, v11
	global_store_dwordx2 v[18:19], v[12:13], off
	s_waitcnt lgkmcnt(0)
	v_mfma_f32_16x16x32_f16 v[10:13], v[30:33], v[0:3], v[34:37]
	s_and_saveexec_b64 s[2:3], s[4:5]
	s_cbranch_execnz .LBB1_25
	s_or_b64 exec, exec, s[2:3]
	s_and_saveexec_b64 s[2:3], s[0:1]
	s_cbranch_execnz .LBB1_26

	.amdhsa_kernel _Z5k_ncaILi0EEvPKDF16_S1_PKfS3_PDF16_S3_S3_S3_S3_Pf
		.amdhsa_group_segment_fixed_size 0
		.amdhsa_private_segment_fixed_size 0
		.amdhsa_kernarg_size 80
		.amdhsa_user_sgpr_count 2
		.amdhsa_user_sgpr_dispatch_ptr 0
		.amdhsa_user_sgpr_queue_ptr 0
		.amdhsa_user_sgpr_kernarg_segment_ptr 1
		.amdhsa_user_sgpr_dispatch_id 0
		.amdhsa_user_sgpr_kernarg_preload_length 0
		.amdhsa_user_sgpr_kernarg_preload_offset 0
		.amdhsa_user_sgpr_private_segment_size 0
		.amdhsa_uses_dynamic_stack 0
		.amdhsa_enable_private_segment 0
		.amdhsa_system_sgpr_workgroup_id_x 1
		.amdhsa_system_sgpr_workgroup_id_y 0
		.amdhsa_system_sgpr_workgroup_id_z 0
		.amdhsa_system_sgpr_workgroup_info 0
		.amdhsa_system_vgpr_workitem_id 0
		.amdhsa_next_free_vgpr 169
		.amdhsa_next_free_sgpr 96
		.amdhsa_accum_offset 132
		.amdhsa_reserve_vcc 1
		.amdhsa_float_round_mode_32 0
		.amdhsa_float_round_mode_16_64 0
		.amdhsa_float_denorm_mode_32 3
		.amdhsa_float_denorm_mode_16_64 3
		.amdhsa_dx10_clamp 1
		.amdhsa_ieee_mode 1
		.amdhsa_fp16_overflow 0
		.amdhsa_tg_split 0
		.amdhsa_exception_fp_ieee_invalid_op 0
		.amdhsa_exception_fp_denorm_src 0
		.amdhsa_exception_fp_ieee_div_zero 0
		.amdhsa_exception_fp_ieee_overflow 0
		.amdhsa_exception_fp_ieee_underflow 0
		.amdhsa_exception_fp_ieee_inexact 0
		.amdhsa_exception_int_div_zero 0
	.end_amdhsa_kernel

.LBB2_26:
	s_or_b64 exec, exec, s[0:1]
	s_add_i32 s0, 0, 0x11880
	s_movk_i32 s1, 0x1600
	v_mov_b32_e32 v6, s0
	v_mad_u32_u24 v7, v26, s1, v6
	v_lshlrev_b32_e32 v8, 2, v38
	v_add_u32_e32 v9, v7, v8
	ds_write2st64_b32 v9, v22, v23 offset1:1
	ds_write2st64_b32 v9, v24, v25 offset0:2 offset1:3
	ds_write2st64_b32 v9, v18, v19 offset0:4 offset1:5
	ds_write2st64_b32 v9, v20, v21 offset0:6 offset1:7
	ds_write2st64_b32 v9, v14, v15 offset0:8 offset1:9
	ds_write2st64_b32 v9, v16, v17 offset0:10 offset1:11
	ds_write2st64_b32 v9, v10, v11 offset0:12 offset1:13
	ds_write2st64_b32 v9, v12, v13 offset0:14 offset1:15
	ds_write2st64_b32 v9, v2, v3 offset0:16 offset1:17
	ds_write2st64_b32 v9, v4, v5 offset0:18 offset1:19
	ds_write_b32 v9, v28 offset:5120
	v_xor_b32_e32 v9, 4, v26
	v_mad_u32_u24 v6, v9, s1, v6
	v_add_u32_e32 v29, v6, v8
	s_waitcnt lgkmcnt(0)
	s_barrier
	ds_read_b32 v8, v29 offset:5120
	v_lshlrev_b32_e32 v27, 2, v59
	v_add_u32_e32 v7, v7, v27
	v_add_u32_e32 v6, v6, v27
	ds_read_b32 v141, v6 offset:4224
	ds_read_b32 v140, v7 offset:4224
	ds_read2st64_b32 v[36:37], v29 offset0:18 offset1:19
	ds_read2st64_b32 v[30:31], v29 offset0:16 offset1:17
	ds_read2st64_b32 v[32:33], v29 offset1:1
	ds_read2st64_b32 v[34:35], v29 offset0:2 offset1:3
	ds_read2st64_b32 v[40:41], v29 offset0:4 offset1:5
	ds_read2st64_b32 v[42:43], v29 offset0:6 offset1:7
	ds_read2st64_b32 v[48:49], v29 offset0:8 offset1:9
	ds_read2st64_b32 v[52:53], v29 offset0:10 offset1:11
	ds_read2st64_b32 v[54:55], v29 offset0:12 offset1:13
	ds_read2st64_b32 v[62:63], v29 offset0:14 offset1:15
	s_waitcnt lgkmcnt(12)
	v_max_f32_e32 v6, v8, v8
	v_max_f32_e32 v7, v28, v28
	v_max_f32_e32 v6, v7, v6
	v_sub_f32_e32 v7, v28, v6
	v_sub_f32_e32 v6, v8, v6
	v_exp_f32_e32 v142, v7
	v_exp_f32_e32 v143, v6
	v_lshl_add_u32 v28, v39, 2, 0
	v_add_u32_e32 v51, 0x10e00, v28
	ds_read_b128 v[6:9], v51
	s_waitcnt lgkmcnt(11)
	v_pk_mul_f32 v[140:141], v[140:141], v[142:143]
	s_nop 0
	v_add_f32_e32 v144, v140, v141
	v_rcp_f32_e32 v144, v144
	s_movk_i32 s0, 0xa0
	s_nop 0
	v_mul_f32_e32 v44, v142, v144
	v_mul_f32_e32 v46, v143, v144
	s_waitcnt lgkmcnt(8)
	v_pk_mul_f32 v[32:33], v[46:47], v[32:33] op_sel_hi:[0,1]
	v_pk_fma_f32 v[22:23], v[44:45], v[22:23], v[32:33] op_sel_hi:[0,1,1]
	v_cvt_pk_f16_f32 v32, v22, v23
	s_waitcnt lgkmcnt(7)
	v_pk_mul_f32 v[22:23], v[46:47], v[34:35] op_sel_hi:[0,1]
	v_pk_fma_f32 v[22:23], v[44:45], v[24:25], v[22:23] op_sel_hi:[0,1,1]
	v_cvt_pk_f16_f32 v33, v22, v23
	s_waitcnt lgkmcnt(6)
	v_pk_mul_f32 v[22:23], v[46:47], v[40:41] op_sel_hi:[0,1]
	v_pk_fma_f32 v[18:19], v[44:45], v[18:19], v[22:23] op_sel_hi:[0,1,1]
	v_cvt_pk_f16_f32 v34, v18, v19
	s_waitcnt lgkmcnt(5)
	v_pk_mul_f32 v[18:19], v[46:47], v[42:43] op_sel_hi:[0,1]
	v_pk_fma_f32 v[18:19], v[44:45], v[20:21], v[18:19] op_sel_hi:[0,1,1]
	v_cvt_pk_f16_f32 v35, v18, v19
	s_waitcnt lgkmcnt(4)
	v_pk_mul_f32 v[18:19], v[46:47], v[48:49] op_sel_hi:[0,1]
	v_pk_fma_f32 v[14:15], v[44:45], v[14:15], v[18:19] op_sel_hi:[0,1,1]
	v_cvt_pk_f16_f32 v40, v14, v15
	s_waitcnt lgkmcnt(3)
	v_pk_mul_f32 v[14:15], v[46:47], v[52:53] op_sel_hi:[0,1]
	v_pk_fma_f32 v[14:15], v[44:45], v[16:17], v[14:15] op_sel_hi:[0,1,1]
	v_cvt_pk_f16_f32 v41, v14, v15
	s_waitcnt lgkmcnt(2)
	v_pk_mul_f32 v[14:15], v[46:47], v[54:55] op_sel_hi:[0,1]
	v_pk_fma_f32 v[10:11], v[44:45], v[10:11], v[14:15] op_sel_hi:[0,1,1]
	v_cvt_pk_f16_f32 v42, v10, v11
	s_waitcnt lgkmcnt(0)
	v_pk_mul_f32 v[10:11], v[46:47], v[62:63] op_sel_hi:[0,1]
	v_pk_fma_f32 v[10:11], v[44:45], v[12:13], v[10:11] op_sel_hi:[0,1,1]
	v_cvt_pk_f16_f32 v43, v10, v11
	v_pk_mul_f32 v[10:11], v[46:47], v[30:31] op_sel_hi:[0,1]
	v_pk_fma_f32 v[2:3], v[44:45], v[2:3], v[10:11] op_sel_hi:[0,1,1]
	v_cvt_pk_f16_f32 v24, v2, v3
	v_pk_mul_f32 v[2:3], v[46:47], v[36:37] op_sel_hi:[0,1]
	v_pk_fma_f32 v[2:3], v[44:45], v[4:5], v[2:3] op_sel_hi:[0,1,1]
	v_or_b32_e32 v30, v39, v60
	v_cvt_pk_f16_f32 v2, v2, v3
	v_cmp_lt_u32_e32 vcc, 31, v38
	v_and_or_b32 v29, v39, 4, v60
	v_mul_u32_u24_e32 v3, 0x50, v30
	v_cndmask_b32_e64 v45, v2, 0, vcc
	v_mad_u32_u24 v2, v29, s0, 0
	v_lshlrev_b32_e32 v36, 3, v59
	v_lshlrev_b32_e32 v48, 1, v3
	v_add_u32_e32 v31, 0xe100, v2
	v_and_b32_e32 v2, 24, v36
	v_add_u32_e32 v49, 0, v48
	v_add_u32_e32 v44, v49, v2
	v_add_u32_e32 v37, v31, v2
	v_add3_u32 v25, 0, v2, v48
	ds_read_b64_tr_b16 v[12:13], v44 offset:60160
	ds_read_b64_tr_b16 v[10:11], v25 offset:57600
	ds_read_b64_tr_b16 v[14:15], v25 offset:62720
	ds_read_b64_tr_b16 v[16:17], v44 offset:65280
	ds_read_b64_tr_b16 v[2:3], v37 offset:10240
	ds_read_b64_tr_b16 v[18:19], v25 offset:57664
	ds_read_b64_tr_b16 v[22:23], v37 offset:10272
	ds_read_b64_tr_b16 v[54:55], v44 offset:60192
	ds_read_b64_tr_b16 v[20:21], v44 offset:60224
	ds_read_b64_tr_b16 v[62:63], v44 offset:60288
	s_waitcnt lgkmcnt(8)
	v_mfma_f32_16x16x32_f16 v[6:9], v[10:13], v[32:35], v[6:9]
	v_mov_b32_e32 v4, 0
	v_mov_b32_e32 v5, v4
	ds_read_b64_tr_b16 v[52:53], v25 offset:57632
	ds_read_b64_tr_b16 v[10:11], v25 offset:62784
	s_waitcnt vmcnt(1)
	ds_read_b64_tr_b16 v[66:67], v44 offset:65312
	ds_read_b64_tr_b16 v[12:13], v44 offset:65344
	ds_read_b64_tr_b16 v[70:71], v44 offset:65408
	s_waitcnt lgkmcnt(11)
	v_mfma_f32_16x16x32_f16 v[6:9], v[14:17], v[40:43], v[6:9]
	v_cndmask_b32_e64 v44, v24, 0, vcc
	v_mov_b32_e32 v46, v4
	v_mov_b32_e32 v47, v4
	v_mov_b32_e32 v24, v4
	v_or_b32_e32 v36, 0x60, v36
	s_waitcnt lgkmcnt(10)
	v_mfma_f32_16x16x32_f16 v[14:17], v[2:5], v[44:47], v[6:9]
	s_nop 2
	ds_read_b128 v[6:9], v51 offset:64
	s_waitcnt vmcnt(0)
	ds_read_b128 v[72:75], v51 offset:128
	ds_read_b64_tr_b16 v[2:3], v37 offset:10304
	ds_read_b64_tr_b16 v[64:65], v25 offset:62752
	ds_read_b64_tr_b16 v[68:69], v25 offset:62848
	ds_read_b64_tr_b16 v[60:61], v25 offset:57728
	v_mov_b32_e32 v25, v4
	s_waitcnt lgkmcnt(5)
	v_mfma_f32_16x16x32_f16 v[6:9], v[52:55], v[32:35], v[6:9]
	v_add3_u32 v48, 0, v36, v48
	v_add_u32_e32 v49, v49, v36
	s_movk_i32 s0, 0xff
	s_waitcnt lgkmcnt(2)
	v_mfma_f32_16x16x32_f16 v[6:9], v[64:67], v[40:43], v[6:9]
	v_cmp_lt_u32_e64 s[0:1], s0, v0
	v_mfma_f32_16x16x32_f16 v[22:25], v[22:25], v[44:47], v[6:9]
	v_mfma_f32_16x16x32_f16 v[6:9], v[18:21], v[32:35], v[72:75]
	ds_read_b64_tr_b16 v[18:19], v48 offset:57600
	ds_read_b64_tr_b16 v[20:21], v49 offset:60160
	v_mfma_f32_16x16x32_f16 v[6:9], v[10:13], v[40:43], v[6:9]
	v_mfma_f32_16x16x32_f16 v[10:13], v[2:5], v[44:47], v[6:9]
	v_add_u32_e32 v2, v31, v36
	s_nop 5
	ds_read_b128 v[6:9], v51 offset:192
	ds_read_b64_tr_b16 v[52:53], v48 offset:62720
	ds_read_b64_tr_b16 v[2:3], v2 offset:10240
	ds_read_b128 v[64:67], v51 offset:256
	ds_read_b64_tr_b16 v[54:55], v49 offset:65280
	s_waitcnt lgkmcnt(4)
	v_mfma_f32_16x16x32_f16 v[6:9], v[18:21], v[32:35], v[6:9]
	s_waitcnt lgkmcnt(0)
	v_mfma_f32_16x16x32_f16 v[6:9], v[52:55], v[40:43], v[6:9]
	v_mfma_f32_16x16x32_f16 v[18:21], v[2:5], v[44:47], v[6:9]
	ds_read_b64_tr_b16 v[2:3], v37 offset:10368
	v_mfma_f32_16x16x32_f16 v[6:9], v[60:63], v[32:35], v[64:67]
	v_mfma_f32_16x16x32_f16 v[6:9], v[68:71], v[40:43], v[6:9]
	s_waitcnt lgkmcnt(0)
	v_mfma_f32_16x16x32_f16 v[6:9], v[2:5], v[44:47], v[6:9]
	s_and_saveexec_b64 s[6:7], s[0:1]
	s_xor_b64 s[0:1], exec, s[6:7]
	s_cbranch_execz .LBB2_38
	v_lshlrev_b32_e32 v5, 2, v1
	s_add_i32 s6, 0, 0x10f40
	v_cvt_pk_f16_f32 v0, v14, v15
	v_add_u32_e32 v14, 0x11840, v28
	v_lshl_add_u32 v5, v5, 1, s6
	v_cvt_pk_f16_f32 v3, v24, v25
	v_cvt_pk_f16_f32 v2, v22, v23
	v_cvt_pk_f16_f32 v15, v20, v21
	v_lshl_add_u32 v28, v30, 5, v5
	ds_read_b128 v[20:23], v14
	ds_read_b64_tr_b16 v[24:25], v28
	ds_read_b64_tr_b16 v[26:27], v28 offset:512
	v_lshl_add_u32 v5, v29, 5, v5
	v_cvt_pk_f16_f32 v1, v16, v17
	v_cvt_pk_f16_f32 v14, v18, v19
	ds_read_b64_tr_b16 v[16:17], v28 offset:1024
	ds_read_b64_tr_b16 v[18:19], v28 offset:1536
	v_cvt_pk_f16_f32 v28, v6, v7
	ds_read_b64_tr_b16 v[6:7], v5 offset:2048
	s_waitcnt lgkmcnt(3)
	v_mfma_f32_16x16x32_f16 v[0:3], v[24:27], v[0:3], v[20:23]
	v_cvt_pk_f16_f32 v13, v12, v13
	v_cvt_pk_f16_f32 v12, v10, v11
	v_cvt_pk_f16_f32 v5, v8, v9
	v_mov_b32_e32 v8, v4
	v_mov_b32_e32 v9, v4
	s_waitcnt lgkmcnt(1)
	v_mfma_f32_16x16x32_f16 v[10:13], v[16:19], v[12:15], v[0:3]
	s_nop 2
	v_cndmask_b32_e64 v3, v5, 0, vcc
	v_cndmask_b32_e64 v2, v28, 0, vcc
	v_mov_b32_e32 v5, v4
	s_waitcnt lgkmcnt(0)
	s_nop 0
	v_mfma_f32_16x16x32_f16 v[0:3], v[6:9], v[2:5], v[10:13]
	s_and_saveexec_b64 s[6:7], s[2:3]
	s_xor_b64 s[2:3], exec, s[6:7]
	s_cbranch_execz .LBB2_35
	v_cmp_ne_u32_e32 vcc, 3, v50
	s_and_saveexec_b64 s[6:7], vcc
	s_cbranch_execz .LBB2_34
	v_cmp_ne_u32_e32 vcc, 1, v50
	s_and_saveexec_b64 s[8:9], vcc
	s_xor_b64 s[8:9], exec, s[8:9]
	v_lshl_add_u32 v4, v56, 1, v56
	v_mov_b32_e32 v5, 0
	v_lshl_add_u64 v[4:5], v[4:5], 2, s[4:5]
	s_mov_b64 s[10:11], 0x70000
	v_lshl_add_u64 v[4:5], v[4:5], 0, s[10:11]
	s_andn2_saveexec_b64 s[8:9], s[8:9]
	v_mul_lo_u32 v4, v56, 7
	v_mov_b32_e32 v5, 0
	v_lshl_add_u64 v[4:5], v[4:5], 2, s[4:5]
	v_lshl_add_u64 v[4:5], v[4:5], 0, 16
	s_or_b64 exec, exec, s[8:9]
	v_max3_f32 v3, v0, v1, v2
	v_sub_f32_e32 v0, v0, v3
	v_sub_f32_e32 v1, v1, v3
	v_mul_f32_e32 v0, 0x3fb8aa3b, v0
	v_mul_f32_e32 v1, 0x3fb8aa3b, v1
	v_sub_f32_e32 v2, v2, v3
	v_exp_f32_e32 v0, v0
	v_exp_f32_e32 v1, v1
	v_mul_f32_e32 v2, 0x3fb8aa3b, v2
	v_exp_f32_e32 v3, v2
	v_add_f32_e32 v2, v0, v1
	v_add_f32_e32 v2, v3, v2
	v_rcp_f32_e32 v2, v2
	s_nop 0
	v_pk_mul_f32 v[0:1], v[0:1], v[2:3] op_sel_hi:[1,0]
	v_mul_f32_e32 v2, v3, v2
	global_store_dwordx3 v[4:5], v[0:2], off nt

	.amdhsa_kernel _Z5k_ncaILi1EEvPKDF16_S1_PKfS3_PDF16_S3_S3_S3_S3_Pf
		.amdhsa_group_segment_fixed_size 0
		.amdhsa_private_segment_fixed_size 0
		.amdhsa_kernarg_size 80
		.amdhsa_user_sgpr_count 2
		.amdhsa_user_sgpr_dispatch_ptr 0
		.amdhsa_user_sgpr_queue_ptr 0
		.amdhsa_user_sgpr_kernarg_segment_ptr 1
		.amdhsa_user_sgpr_dispatch_id 0
		.amdhsa_user_sgpr_kernarg_preload_length 0
		.amdhsa_user_sgpr_kernarg_preload_offset 0
		.amdhsa_user_sgpr_private_segment_size 0
		.amdhsa_uses_dynamic_stack 0
		.amdhsa_enable_private_segment 0
		.amdhsa_system_sgpr_workgroup_id_x 1
		.amdhsa_system_sgpr_workgroup_id_y 0
		.amdhsa_system_sgpr_workgroup_id_z 0
		.amdhsa_system_sgpr_workgroup_info 0
		.amdhsa_system_vgpr_workitem_id 0
		.amdhsa_next_free_vgpr 169
		.amdhsa_next_free_sgpr 96
		.amdhsa_accum_offset 148
		.amdhsa_reserve_vcc 1
		.amdhsa_float_round_mode_32 0
		.amdhsa_float_round_mode_16_64 0
		.amdhsa_float_denorm_mode_32 3
		.amdhsa_float_denorm_mode_16_64 3
		.amdhsa_dx10_clamp 1
		.amdhsa_ieee_mode 1
		.amdhsa_fp16_overflow 0
		.amdhsa_tg_split 0
		.amdhsa_exception_fp_ieee_invalid_op 0
		.amdhsa_exception_fp_denorm_src 0
		.amdhsa_exception_fp_ieee_div_zero 0
		.amdhsa_exception_fp_ieee_overflow 0
		.amdhsa_exception_fp_ieee_underflow 0
		.amdhsa_exception_fp_ieee_inexact 0
		.amdhsa_exception_int_div_zero 0
	.end_amdhsa_kernel
